# MoE k-loop: leading wave group no longer drains lgkmcnt before its staging barrier (drain moved in front of the post-burst barrier)
# baseline (speedup 1.0000x reference)
.LBB0_1174:
	s_setprio 0
	s_add_i32 s5, s5, 1
	s_and_b32 s5, s5, 3
	s_add_i32 s35, s2, 1
	s_waitcnt lgkmcnt(0)
	s_barrier
	s_cmp_lg_u32 s2, 2
	s_cselect_b32 s2, s35, 0
	s_add_i32 s34, s34, 1
	v_lshl_add_u64 v[204:205], v[204:205], 0, 64
	v_lshl_add_u64 v[206:207], v[206:207], 0, 64
	v_lshl_add_u64 v[208:209], v[208:209], 0, s[66:67]
.LBB0_1175:
	s_bitcmp0_b32 s34, 0
	s_cselect_b32 s8, s91, 0x10000
	s_cselect_b32 s9, 0x10000, s91
	s_add_i32 s8, s8, 0
	v_add_u32_e32 v1, s8, v214
	v_add_u32_e32 v3, s8, v217
	s_waitcnt lgkmcnt(14)
	ds_read_b64_tr_b16 v[150:151], v1
	ds_read_b64_tr_b16 v[152:153], v1 offset:2048
	ds_read_b64_tr_b16 v[154:155], v3
	ds_read_b64_tr_b16 v[156:157], v3 offset:2048
	v_add_u32_e32 v1, s8, v216
	v_add_u32_e32 v3, s8, v215
	s_waitcnt lgkmcnt(14)
	ds_read_b64_tr_b16 v[158:159], v1
	ds_read_b64_tr_b16 v[160:161], v1 offset:2048
	ds_read_b64_tr_b16 v[162:163], v3
	ds_read_b64_tr_b16 v[164:165], v3 offset:2048
	s_lshl_b32 s35, s5, 14
	s_cmp_eq_u32 s5, 3
	s_cselect_b32 s35, 0x18000, s35
	v_add_u32_e32 v1, s35, v213
	s_waitcnt lgkmcnt(14)
	ds_read_b128 v[194:197], v1
	ds_read_b128 v[190:193], v1 offset:1024
	ds_read_b128 v[186:189], v1 offset:2048
	ds_read_b128 v[182:185], v1 offset:3072
	s_waitcnt lgkmcnt(14)
	ds_read_b128 v[178:181], v1 offset:4096
	ds_read_b128 v[174:177], v1 offset:5120
	ds_read_b128 v[170:173], v1 offset:6144
	ds_read_b128 v[166:169], v1 offset:7168
	s_cmp_eq_u32 s5, 0
	s_cselect_b32 s8, 0x8000, 0
	s_add_i32 s8, s33, s8
	s_mov_b32 s35, m0
	s_mov_b32 m0, s8
	s_nop 0
	global_load_lds_dwordx4 v[206:207], off
	s_mov_b32 m0, s35
	s_addk_i32 s8, 0x2000
	s_mov_b32 s35, m0
	s_mov_b32 m0, s8
	s_nop 0
	global_load_lds_dwordx4 v[204:205], off
	s_mov_b32 m0, s35
	s_cmp_eq_u32 s5, 0
	s_cselect_b32 s8, 0x14000, 0
	s_add_i32 s8, s33, s8
	s_addk_i32 s8, 0x3fc0
	s_mov_b32 s35, m0
	s_mov_b32 m0, s8
	s_nop 0
	global_load_lds_dwordx4 v[206:207], off offset:64
	s_mov_b32 m0, s35
	s_addk_i32 s8, 0x2000
	s_mov_b32 s35, m0
	s_mov_b32 m0, s8
	s_nop 0
	global_load_lds_dwordx4 v[204:205], off offset:64
	s_mov_b32 m0, s35
	v_add_u32_e32 v1, s9, v218
	s_waitcnt vmcnt(8)
	s_nop 0
	v_cvt_pk_bf16_f32 v224, v224, v225
	v_cvt_pk_bf16_f32 v225, v226, v227
	v_cvt_pk_bf16_f32 v226, v228, v229
	v_cvt_pk_bf16_f32 v227, v230, v231
	ds_write_b128 v1, v[224:227]
	v_cvt_pk_bf16_f32 v232, v232, v233
	v_cvt_pk_bf16_f32 v233, v234, v235
	v_cvt_pk_bf16_f32 v234, v236, v237
	v_cvt_pk_bf16_f32 v235, v238, v239
	ds_write_b128 v1, v[232:235] offset:8192
	global_load_dwordx4 v[224:227], v[208:209], off
	global_load_dwordx4 v[228:231], v[208:209], off offset:16
	v_lshl_add_u64 v[4:5], v[208:209], 0, s[62:63]
	global_load_dwordx4 v[232:235], v[4:5], off
	global_load_dwordx4 v[236:239], v[4:5], off offset:16
	s_and_b64 vcc, exec, s[10:11]
	s_cbranch_vccnz .Lmoe_nodrain_0
	s_waitcnt lgkmcnt(0)
.Lmoe_nodrain_0:
	s_barrier
	s_setprio 1
	v_cndmask_b32_e64 v1, 0, 1, s[76:77]
	v_cmp_ne_u32_e64 s[8:9], 1, v1
	s_andn2_b64 vcc, exec, s[76:77]
	s_cbranch_vccnz .Lmoe_end_even
	s_waitcnt lgkmcnt(9)
	v_mfma_f32_16x16x32_bf16 v[146:149], v[150:153], v[194:197], v[146:149]
	v_mfma_f32_16x16x32_bf16 v[142:145], v[154:157], v[194:197], v[142:145]
	v_mfma_f32_16x16x32_bf16 v[138:141], v[158:161], v[194:197], v[138:141]
	v_mfma_f32_16x16x32_bf16 v[134:137], v[162:165], v[194:197], v[134:137]
	s_waitcnt lgkmcnt(8)
	v_mfma_f32_16x16x32_bf16 v[130:133], v[150:153], v[190:193], v[130:133]
	v_mfma_f32_16x16x32_bf16 v[122:125], v[154:157], v[190:193], v[122:125]
	v_mfma_f32_16x16x32_bf16 v[126:129], v[158:161], v[190:193], v[126:129]
	v_mfma_f32_16x16x32_bf16 v[118:121], v[162:165], v[190:193], v[118:121]
	s_waitcnt lgkmcnt(7)
	v_mfma_f32_16x16x32_bf16 v[114:117], v[150:153], v[186:189], v[114:117]
	v_mfma_f32_16x16x32_bf16 v[106:109], v[154:157], v[186:189], v[106:109]
	v_mfma_f32_16x16x32_bf16 v[110:113], v[158:161], v[186:189], v[110:113]
	v_mfma_f32_16x16x32_bf16 v[102:105], v[162:165], v[186:189], v[102:105]
	s_waitcnt lgkmcnt(6)
	v_mfma_f32_16x16x32_bf16 v[98:101], v[150:153], v[182:185], v[98:101]
	v_mfma_f32_16x16x32_bf16 v[90:93], v[154:157], v[182:185], v[90:93]
	v_mfma_f32_16x16x32_bf16 v[94:97], v[158:161], v[182:185], v[94:97]
	v_mfma_f32_16x16x32_bf16 v[86:89], v[162:165], v[182:185], v[86:89]
	s_waitcnt lgkmcnt(5)
	v_mfma_f32_16x16x32_bf16 v[82:85], v[150:153], v[178:181], v[82:85]
	v_mfma_f32_16x16x32_bf16 v[74:77], v[154:157], v[178:181], v[74:77]
	v_mfma_f32_16x16x32_bf16 v[78:81], v[158:161], v[178:181], v[78:81]
	v_mfma_f32_16x16x32_bf16 v[70:73], v[162:165], v[178:181], v[70:73]
	s_waitcnt lgkmcnt(4)
	v_mfma_f32_16x16x32_bf16 v[66:69], v[150:153], v[174:177], v[66:69]
	v_mfma_f32_16x16x32_bf16 v[58:61], v[154:157], v[174:177], v[58:61]
	v_mfma_f32_16x16x32_bf16 v[62:65], v[158:161], v[174:177], v[62:65]
	v_mfma_f32_16x16x32_bf16 v[54:57], v[162:165], v[174:177], v[54:57]
	s_waitcnt lgkmcnt(3)
	v_mfma_f32_16x16x32_bf16 v[50:53], v[150:153], v[170:173], v[50:53]
	v_mfma_f32_16x16x32_bf16 v[42:45], v[154:157], v[170:173], v[42:45]
	v_mfma_f32_16x16x32_bf16 v[46:49], v[158:161], v[170:173], v[46:49]
	v_mfma_f32_16x16x32_bf16 v[38:41], v[162:165], v[170:173], v[38:41]
	s_waitcnt lgkmcnt(2)
	v_mfma_f32_16x16x32_bf16 v[34:37], v[150:153], v[166:169], v[34:37]
	v_mfma_f32_16x16x32_bf16 v[26:29], v[154:157], v[166:169], v[26:29]
	v_mfma_f32_16x16x32_bf16 v[30:33], v[158:161], v[166:169], v[30:33]
	v_mfma_f32_16x16x32_bf16 v[22:25], v[162:165], v[166:169], v[22:25]
.Lmoe_end_even:
	s_setprio 0
	s_add_i32 s5, s5, 1
	s_and_b32 s5, s5, 3
	s_add_i32 s35, s2, 1
	s_waitcnt lgkmcnt(0)
	s_barrier
	s_cmp_lg_u32 s2, 2
	s_cselect_b32 s2, s35, 0
	s_add_i32 s34, s34, 1
	v_lshl_add_u64 v[204:205], v[204:205], 0, 64
	v_lshl_add_u64 v[206:207], v[206:207], 0, 64
	v_lshl_add_u64 v[208:209], v[208:209], 0, s[66:67]
	s_cmp_eq_u32 s34, 61
	s_cbranch_scc1 .Lmoe_t61
	s_bitcmp0_b32 s34, 0
	s_cselect_b32 s8, s91, 0x10000
	s_cselect_b32 s9, 0x10000, s91
	s_add_i32 s8, s8, 0
	v_add_u32_e32 v1, s8, v214
	v_add_u32_e32 v3, s8, v217
	s_waitcnt lgkmcnt(14)
	ds_read_b64_tr_b16 v[150:151], v1
	ds_read_b64_tr_b16 v[152:153], v1 offset:2048
	ds_read_b64_tr_b16 v[154:155], v3
	ds_read_b64_tr_b16 v[156:157], v3 offset:2048
	v_add_u32_e32 v1, s8, v216
	v_add_u32_e32 v3, s8, v215
	s_waitcnt lgkmcnt(14)
	ds_read_b64_tr_b16 v[158:159], v1
	ds_read_b64_tr_b16 v[160:161], v1 offset:2048
	ds_read_b64_tr_b16 v[162:163], v3
	ds_read_b64_tr_b16 v[164:165], v3 offset:2048
	s_lshl_b32 s35, s5, 14
	s_cmp_eq_u32 s5, 3
	s_cselect_b32 s35, 0x18000, s35
	v_add_u32_e32 v1, s35, v213
	s_waitcnt lgkmcnt(14)
	ds_read_b128 v[194:197], v1
	ds_read_b128 v[190:193], v1 offset:1024
	ds_read_b128 v[186:189], v1 offset:2048
	ds_read_b128 v[182:185], v1 offset:3072
	s_waitcnt lgkmcnt(14)
	ds_read_b128 v[178:181], v1 offset:4096
	ds_read_b128 v[174:177], v1 offset:5120
	ds_read_b128 v[170:173], v1 offset:6144
	ds_read_b128 v[166:169], v1 offset:7168
	v_add_u32_e32 v1, s9, v218
	s_waitcnt vmcnt(6)
	s_nop 0
	v_cvt_pk_bf16_f32 v18, v18, v19
	v_cvt_pk_bf16_f32 v19, v20, v21
	v_cvt_pk_bf16_f32 v20, v14, v15
	v_cvt_pk_bf16_f32 v21, v16, v17
	ds_write_b128 v1, v[18:21]
	v_cvt_pk_bf16_f32 v4, v10, v11
	v_cvt_pk_bf16_f32 v5, v12, v13
	v_cvt_pk_bf16_f32 v6, v6, v7
	v_cvt_pk_bf16_f32 v7, v8, v9
	ds_write_b128 v1, v[4:7] offset:8192
	global_load_dwordx4 v[18:21], v[208:209], off
	global_load_dwordx4 v[14:17], v[208:209], off offset:16
	v_lshl_add_u64 v[4:5], v[208:209], 0, s[62:63]
	global_load_dwordx4 v[10:13], v[4:5], off
	global_load_dwordx4 v[6:9], v[4:5], off offset:16
	s_and_b64 vcc, exec, s[10:11]
	s_cbranch_vccnz .Lmoe_nodrain_1
	s_waitcnt lgkmcnt(0)
.Lmoe_nodrain_1:
	s_barrier
	s_setprio 1
	v_cndmask_b32_e64 v1, 0, 1, s[76:77]
	v_cmp_ne_u32_e64 s[8:9], 1, v1
	s_andn2_b64 vcc, exec, s[76:77]
	s_cbranch_vccnz .LBB0_1174
	s_waitcnt lgkmcnt(9)
	v_mfma_f32_16x16x32_bf16 v[146:149], v[150:153], v[194:197], v[146:149]
	v_mfma_f32_16x16x32_bf16 v[142:145], v[154:157], v[194:197], v[142:145]
	v_mfma_f32_16x16x32_bf16 v[138:141], v[158:161], v[194:197], v[138:141]
	v_mfma_f32_16x16x32_bf16 v[134:137], v[162:165], v[194:197], v[134:137]
	s_waitcnt lgkmcnt(8)
	v_mfma_f32_16x16x32_bf16 v[130:133], v[150:153], v[190:193], v[130:133]
	v_mfma_f32_16x16x32_bf16 v[122:125], v[154:157], v[190:193], v[122:125]
	v_mfma_f32_16x16x32_bf16 v[126:129], v[158:161], v[190:193], v[126:129]
	v_mfma_f32_16x16x32_bf16 v[118:121], v[162:165], v[190:193], v[118:121]
	s_waitcnt lgkmcnt(7)
	v_mfma_f32_16x16x32_bf16 v[114:117], v[150:153], v[186:189], v[114:117]
	v_mfma_f32_16x16x32_bf16 v[106:109], v[154:157], v[186:189], v[106:109]
	v_mfma_f32_16x16x32_bf16 v[110:113], v[158:161], v[186:189], v[110:113]
	v_mfma_f32_16x16x32_bf16 v[102:105], v[162:165], v[186:189], v[102:105]
	s_waitcnt lgkmcnt(6)
	v_mfma_f32_16x16x32_bf16 v[98:101], v[150:153], v[182:185], v[98:101]
	v_mfma_f32_16x16x32_bf16 v[90:93], v[154:157], v[182:185], v[90:93]
	v_mfma_f32_16x16x32_bf16 v[94:97], v[158:161], v[182:185], v[94:97]
	v_mfma_f32_16x16x32_bf16 v[86:89], v[162:165], v[182:185], v[86:89]
	s_waitcnt lgkmcnt(5)
	v_mfma_f32_16x16x32_bf16 v[82:85], v[150:153], v[178:181], v[82:85]
	v_mfma_f32_16x16x32_bf16 v[74:77], v[154:157], v[178:181], v[74:77]
	v_mfma_f32_16x16x32_bf16 v[78:81], v[158:161], v[178:181], v[78:81]
	v_mfma_f32_16x16x32_bf16 v[70:73], v[162:165], v[178:181], v[70:73]
	s_waitcnt lgkmcnt(4)
	v_mfma_f32_16x16x32_bf16 v[66:69], v[150:153], v[174:177], v[66:69]
	v_mfma_f32_16x16x32_bf16 v[58:61], v[154:157], v[174:177], v[58:61]
	v_mfma_f32_16x16x32_bf16 v[62:65], v[158:161], v[174:177], v[62:65]
	v_mfma_f32_16x16x32_bf16 v[54:57], v[162:165], v[174:177], v[54:57]
	s_waitcnt lgkmcnt(3)
	v_mfma_f32_16x16x32_bf16 v[50:53], v[150:153], v[170:173], v[50:53]
	v_mfma_f32_16x16x32_bf16 v[42:45], v[154:157], v[170:173], v[42:45]
	v_mfma_f32_16x16x32_bf16 v[46:49], v[158:161], v[170:173], v[46:49]
	v_mfma_f32_16x16x32_bf16 v[38:41], v[162:165], v[170:173], v[38:41]
	s_waitcnt lgkmcnt(2)
	v_mfma_f32_16x16x32_bf16 v[34:37], v[150:153], v[166:169], v[34:37]
	v_mfma_f32_16x16x32_bf16 v[26:29], v[154:157], v[166:169], v[26:29]
	v_mfma_f32_16x16x32_bf16 v[30:33], v[158:161], v[166:169], v[30:33]
	v_mfma_f32_16x16x32_bf16 v[22:25], v[162:165], v[166:169], v[22:25]
	s_branch .LBB0_1174
.Lmoe_t61:
	s_bitcmp0_b32 s34, 0
	s_cselect_b32 s8, s91, 0x10000
	s_cselect_b32 s9, 0x10000, s91
	s_add_i32 s8, s8, 0
	v_add_u32_e32 v1, s8, v214
	v_add_u32_e32 v3, s8, v217
	s_waitcnt lgkmcnt(14)
	ds_read_b64_tr_b16 v[150:151], v1
	ds_read_b64_tr_b16 v[152:153], v1 offset:2048
	ds_read_b64_tr_b16 v[154:155], v3
	ds_read_b64_tr_b16 v[156:157], v3 offset:2048
	v_add_u32_e32 v1, s8, v216
	v_add_u32_e32 v3, s8, v215
	s_waitcnt lgkmcnt(14)
	ds_read_b64_tr_b16 v[158:159], v1
	ds_read_b64_tr_b16 v[160:161], v1 offset:2048
	ds_read_b64_tr_b16 v[162:163], v3
	ds_read_b64_tr_b16 v[164:165], v3 offset:2048
	s_lshl_b32 s35, s5, 14
	s_cmp_eq_u32 s5, 3
	s_cselect_b32 s35, 0x18000, s35
	v_add_u32_e32 v1, s35, v213
	s_waitcnt lgkmcnt(14)
	ds_read_b128 v[194:197], v1
	ds_read_b128 v[190:193], v1 offset:1024
	ds_read_b128 v[186:189], v1 offset:2048
	ds_read_b128 v[182:185], v1 offset:3072
	s_waitcnt lgkmcnt(14)
	ds_read_b128 v[178:181], v1 offset:4096
	ds_read_b128 v[174:177], v1 offset:5120
	ds_read_b128 v[170:173], v1 offset:6144
	ds_read_b128 v[166:169], v1 offset:7168
	v_add_u32_e32 v1, s9, v218
	s_waitcnt vmcnt(6)
	s_nop 0
	v_cvt_pk_bf16_f32 v18, v18, v19
	v_cvt_pk_bf16_f32 v19, v20, v21
	v_cvt_pk_bf16_f32 v20, v14, v15
	v_cvt_pk_bf16_f32 v21, v16, v17
	ds_write_b128 v1, v[18:21]
	v_cvt_pk_bf16_f32 v4, v10, v11
	v_cvt_pk_bf16_f32 v5, v12, v13
	v_cvt_pk_bf16_f32 v6, v6, v7
	v_cvt_pk_bf16_f32 v7, v8, v9
	ds_write_b128 v1, v[4:7] offset:8192
	s_and_b64 vcc, exec, s[10:11]
	s_cbranch_vccnz .Lmoe_nodrain_2
	s_waitcnt lgkmcnt(0)
